# router prologue waits for one LDS read before the loop issues eight more (never more than 15 LDS ops outstanding) + LRU1 scan reads issued together; on top of router loop rewrite
# speedup vs baseline: 1.0049x; 1.0015x over previous
; #define LAS __attribute__((address_space(3)))
; __device__ __forceinline__ void ln1_router_phase(const Args& a, Frame& F, int l) {
;     ...
; #pragma unroll 1
;         for (int e = 0; e < 16; ++e) { float sA = 0.f, sB = 0.f;
; #pragma unroll
;             for (int j = 0; j < 4; ++j) { const f32x4 w0 = *(const LAS f32x4*)(wl + e * DM + 8 * lane + 512 * j), w1 = *(const LAS f32x4*)(wl + e * DM + 8 * lane + 512 * j + 4);
;                 sA += (va[j][0] * w0[0] + va[j][1] * w0[1]) + (va[j][2] * w0[2] + va[j][3] * w0[3]) + (va[j][4] * w1[0] + va[j][5] * w1[1]) + (va[j][6] * w1[2] + va[j][7] * w1[3]);
;                 sB += (vb[j][0] * w0[0] + vb[j][1] * w0[1]) + (vb[j][2] * w0[2] + vb[j][3] * w0[3]) + (vb[j][4] * w1[0] + vb[j][5] * w1[1]) + (vb[j][6] * w1[2] + vb[j][7] * w1[3]); }
;             sA = wave_sum(sA); sB = wave_sum(sB); lgA = (lane == e) ? sA : lgA; lgB = (lane == e) ? sB : lgB; }
.LBB0_808:
	s_nop 1
	v_mov_b32_e32 v86, 0
	s_mov_b32 s0, 0
	v_mov_b32_e32 v87, 0
	v_add_u32_e32 v99, s0, v0
	ds_read_b128 v[148:151], v99
	ds_read_b128 v[152:155], v99 offset:16
	ds_read_b128 v[156:159], v99 offset:2048
	ds_read_b128 v[160:163], v99 offset:2064
	ds_read_b128 v[164:167], v99 offset:4096
	ds_read_b128 v[168:171], v99 offset:4112
	ds_read_b128 v[172:175], v99 offset:6144
	ds_read_b128 v[176:179], v99 offset:6160
	s_waitcnt lgkmcnt(7)
